# v39 + MoE pre-phase (expert sub-list scan before the expert GEMMs): the four experts' count loads of a wave issued up front (one round trip instead of four)
# speedup vs baseline: 1.0051x; 1.0051x over previous
; #define LAS __attribute__((address_space(3)))
; __global__ void __launch_bounds__(NWAVES * 64, 2) mega_fwd(KArgs args) {
;     ...
;             for (int q = 0; q < 4; ++q) {
;                 const int e = wave * 4 + q; const unsigned* cg = ctl + CW_CNT + 8192 * L + e * NSUB + 4 * lane; unsigned c[4];
; #pragma unroll
;                 for (int j = 0; j < 4; ++j) c[j] = __hip_atomic_load(cg + j, RLX_AGENT);
;                 const unsigned tot = (c[0] + c[1]) + (c[2] + c[3]); unsigned inc = tot;
; #pragma unroll
;                 for (int o = 1; o < 64; o <<= 1) { const unsigned nb = __shfl_up(inc, o); if (lane >= o) inc += nb; }
;                 unsigned run = inc - tot; LAS unsigned short* so = suboL + e * (NSUB + 1) + 4 * lane;
.LBB0_1881:
	v_readlane_b32 s12, v253, 10
	v_and_b32_e32 v4, 64, v237
	v_add_u32_e32 v8, -1, v237
	v_readlane_b32 s13, v253, 11
	v_mov_b32_e32 v9, v0
	v_cmp_lt_i32_e32 vcc, v8, v4
	s_waitcnt lgkmcnt(0)
	v_add_u32_e32 v7, -2, v237
	v_add_u32_e32 v6, -4, v237
	v_readfirstlane_b32 s4, v9
	v_cndmask_b32_e32 v1, v8, v237, vcc
	v_cmp_lt_i32_e32 vcc, v7, v4
	s_ashr_i32 s5, s4, 4
	v_lshlrev_b32_e32 v11, 2, v1
	v_cndmask_b32_e32 v1, v7, v237, vcc
	v_cmp_lt_i32_e32 vcc, v6, v4
	v_add_u32_e32 v3, -8, v237
	v_lshlrev_b32_e32 v12, 2, v1
	v_cndmask_b32_e32 v1, v6, v237, vcc
	v_cmp_lt_i32_e32 vcc, v3, v4
	s_lshr_b32 s7, s5, 2
	s_mov_b32 s2, 0
	v_lshlrev_b32_e32 v13, 2, v1
	v_cndmask_b32_e32 v1, v3, v237, vcc
	s_lshl_b32 s6, s7, 4
	v_lshlrev_b32_e32 v14, 2, v1
	v_add_u32_e32 v1, -16, v237
	s_mul_i32 s5, s7, 0x808
	s_add_i32 s6, s2, s6
	s_lshl_b32 s18, s7, 10
	v_cmp_lt_i32_e32 vcc, v1, v4
	s_add_i32 s5, s2, s5
	s_add_i32 s6, s6, 0
	s_mov_b32 s91, s9
	s_ashr_i32 s19, s18, 31
	v_cndmask_b32_e32 v5, v1, v237, vcc
	s_add_i32 s5, s5, 0
	s_add_i32 s6, s6, 0x20200
	s_lshl_b64 s[14:15], s[90:91], 15
	s_lshl_b64 s[18:19], s[18:19], 2
	v_lshlrev_b32_e32 v15, 2, v5
	v_subrev_u32_e32 v5, 32, v237
	s_add_u32 s7, s12, s18
	v_cmp_lt_i32_e32 vcc, v5, v4
	s_addc_u32 s8, s13, s19
	v_and_b32_e32 v10, 63, v9
	v_cndmask_b32_e32 v4, v5, v237, vcc
	s_add_u32 s12, s7, s14
	v_lshlrev_b32_e32 v16, 2, v4
	v_mov_b32_e32 v4, 0x22402
	v_lshlrev_b32_e32 v130, 4, v10
	s_addc_u32 s13, s8, s15
	v_lshl_or_b32 v17, v10, 3, v4
	v_lshl_add_u64 v[4:5], s[12:13], 0, v[130:131]
	s_mov_b64 s[12:13], 0xc3508
	s_mov_b32 s3, 0
	v_cmp_eq_u32_e64 s[22:23], 0, v10
	v_cmp_gt_u32_e64 s[24:25], 2, v10
	v_cmp_gt_u32_e64 s[26:27], 4, v10
	v_cmp_gt_u32_e64 s[28:29], 8, v10
	v_cmp_gt_u32_e64 s[30:31], 16, v10
	v_cmp_gt_u32_e32 vcc, 32, v10
	v_lshl_add_u64 v[4:5], v[4:5], 0, s[12:13]
	global_load_dword v48, v[4:5], off offset:-8 sc1
	global_load_dword v49, v[4:5], off offset:-4 sc1
	global_load_dword v50, v[4:5], off sc1
	global_load_dword v51, v[4:5], off offset:4 sc1
	global_load_dword v52, v[4:5], off offset:1016 sc1
	global_load_dword v53, v[4:5], off offset:1020 sc1
	global_load_dword v54, v[4:5], off offset:1024 sc1
	global_load_dword v55, v[4:5], off offset:1028 sc1
	global_load_dword v56, v[4:5], off offset:2040 sc1
	global_load_dword v57, v[4:5], off offset:2044 sc1
	global_load_dword v58, v[4:5], off offset:2048 sc1
	global_load_dword v59, v[4:5], off offset:2052 sc1
	global_load_dword v60, v[4:5], off offset:3064 sc1
	global_load_dword v61, v[4:5], off offset:3068 sc1
	global_load_dword v62, v[4:5], off offset:3072 sc1
	global_load_dword v63, v[4:5], off offset:3076 sc1
	s_branch .LBB0_1884

; #define LAS __attribute__((address_space(3)))
; __global__ void __launch_bounds__(NWAVES * 64, 2) mega_fwd(KArgs args) {
;     ...
;                 const int e = wave * 4 + q; const unsigned* cg = ctl + CW_CNT + 8192 * L + e * NSUB + 4 * lane; unsigned c[4];
; #pragma unroll
;                 for (int j = 0; j < 4; ++j) c[j] = __hip_atomic_load(cg + j, RLX_AGENT);
;                 const unsigned tot = (c[0] + c[1]) + (c[2] + c[3]); unsigned inc = tot;
; #pragma unroll
;                 for (int o = 1; o < 64; o <<= 1) { const unsigned nb = __shfl_up(inc, o); if (lane >= o) inc += nb; }
;                 unsigned run = inc - tot; LAS unsigned short* so = suboL + e * (NSUB + 1) + 4 * lane;
; #pragma unroll
;                 for (int j = 0; j < 4; ++j) { run += c[j]; so[j + 1] = (unsigned short)run; }
;                 if (lane == 0) suboL[e * (NSUB + 1)] = 0; if (lane == 63) cntL[e] = run; }
.LBB0_1884:
	s_mov_b32 s7, 0x5040100
	v_cmp_lt_i32_e64 s[34:35], 62, v10
	s_waitcnt vmcnt(0)
	v_mov_b32_e32 v18, v48
	v_mov_b32_e32 v19, v49
	v_mov_b32_e32 v20, v50
	v_mov_b32_e32 v21, v51
	v_mov_b32_e32 v48, v52
	v_mov_b32_e32 v49, v53
	v_mov_b32_e32 v50, v54
	v_mov_b32_e32 v51, v55
	v_mov_b32_e32 v52, v56
	v_mov_b32_e32 v53, v57
	v_mov_b32_e32 v54, v58
	v_mov_b32_e32 v55, v59
	v_mov_b32_e32 v56, v60
	v_mov_b32_e32 v57, v61
	v_mov_b32_e32 v58, v62
	v_mov_b32_e32 v59, v63
	v_add_u32_e32 v22, v19, v18
	v_add3_u32 v22, v22, v20, v21
	ds_bpermute_b32 v23, v11, v22
	s_waitcnt lgkmcnt(0)
	v_cndmask_b32_e64 v23, v23, 0, s[22:23]
	v_add_u32_e32 v23, v23, v22
	ds_bpermute_b32 v24, v12, v23
	s_waitcnt lgkmcnt(0)
	v_cndmask_b32_e64 v24, v24, 0, s[24:25]
	v_add_u32_e32 v23, v24, v23
	ds_bpermute_b32 v24, v13, v23
	s_waitcnt lgkmcnt(0)
	v_cndmask_b32_e64 v24, v24, 0, s[26:27]
	v_add_u32_e32 v23, v24, v23
	ds_bpermute_b32 v24, v14, v23
	s_waitcnt lgkmcnt(0)
	v_cndmask_b32_e64 v24, v24, 0, s[28:29]
	v_add_u32_e32 v23, v24, v23
	ds_bpermute_b32 v24, v15, v23
	s_waitcnt lgkmcnt(0)
	v_cndmask_b32_e64 v24, v24, 0, s[30:31]
	v_add_u32_e32 v23, v24, v23
	ds_bpermute_b32 v24, v16, v23
	s_waitcnt lgkmcnt(0)
	v_cndmask_b32_e64 v24, v24, 0, vcc
	v_add_u32_e32 v23, v24, v23
	v_sub_u32_e32 v22, v23, v22
	v_add_u32_e32 v22, v18, v22
	v_add_u32_e32 v19, v19, v22
	v_add_u32_e32 v24, v20, v19
	v_add_u32_e32 v18, v21, v24
	v_add_u32_e32 v23, s5, v17
	v_perm_b32 v20, v19, v22, s7
	v_perm_b32 v21, v18, v24, s7
	ds_write_b64 v23, v[20:21]
	s_and_saveexec_b64 s[12:13], s[34:35]
	s_xor_b64 s[12:13], exec, s[12:13]
	s_add_i32 s7, s6, s3
	v_mov_b32_e32 v19, s7
	ds_write_b32 v19, v18
	s_andn2_saveexec_b64 s[12:13], s[12:13]
	s_cbranch_execz .LBB0_1883
	v_cmp_eq_u32_e64 s[34:35], 0, v10
	s_and_saveexec_b64 s[14:15], s[34:35]
	s_cbranch_execz .LBB0_1882
	s_add_i32 s7, s5, 0x22400
	v_mov_b32_e32 v18, s7
	ds_write_b16 v18, v131
	s_branch .LBB0_1882
